# P0 expert-weight items remapped so a workgroup's 8 waves take consecutive k-blocks (contiguous 1 KB destination runs) instead of consecutive column blocks
# baseline (speedup 1.0000x reference)
; __device__ __forceinline__ void p0_prologue(Frame& F) {
;     ...
;             const int l = 1 - it / ITEMS_LAYER; int r = ITEMS_LAYER - 1 - it % ITEMS_LAYER;
;             bf16* WL = (bf16*)(F.ws + WS_W + (size_t)l * W_LAYER);
;             if (r < ITEMS_IN) { const float* Fw_in = inptr<const float>(F, I_WIN); const int kb = r / 96, nb = r % 96;
;                 p0_transpose_item(Fw_in + (size_t)l * D * INW, INW, 64 * kb, 64 * nb, WL + W_IN_OFF / 2, in_dest_row(64 * nb), in_dest_row(64 * nb + 32), D, scr, F.lane); continue; }
;             r -= ITEMS_IN;
;             if (r < ITEMS_OUT) { const int kb = r / 64, nb = r % 64; const float* Fw_out = inptr<const float>(F, I_WOUT);
;                 p0_transpose_item8<false>(Fw_out + (size_t)l * D * D, D, 128 * kb, 32 * nb, F.ws + WS_W + (size_t)l * W_LAYER + W_OUT_OFF, (size_t)(32 * nb), D, (float)(1 << WSHIFT), scr, F.lane); continue; }
;             r -= ITEMS_OUT;
;             const int e = r / ITEMS_E, q = r % ITEMS_E;
;             unsigned char* WLb = F.ws + WS_W + (size_t)l * W_LAYER;
;             if (q < 512) { const int up = q >> 8, qq = q & 255, kb = qq / 16, nb = qq % 16, n0 = 32 * nb;
;                 const float* src = (e < NE) ? (inptr<const float>(F, up ? I_WEU : I_WEG) + ((size_t)l * NE + e) * D * EH) : (inptr<const float>(F, up ? I_WSU : I_WSG) + (size_t)l * D * EH);
;                 const size_t dr = (size_t)e * 1024 + (n0 >> 7) * 256 + up * 128 + (n0 & 127);
;                 p0_transpose_item8<false>(src, EH, 128 * kb, n0, WLb + W_1_OFF, dr, D, (float)(1 << WSHIFT), scr, F.lane);
;             } else { const int qq = q - 512, kb = qq / 64, nb = qq % 64;
;                 const float* src = (e < NE) ? (inptr<const float>(F, I_WED) + ((size_t)l * NE + e) * EH * D) : (inptr<const float>(F, I_WSD) + (size_t)l * EH * D);
;                 { const int n0 = 32 * nb, o = n0 & 255; p0_transpose_item8<true>(src, D, 128 * kb, n0, WLb + W_2_OFF, (size_t)e * 2048 + (n0 & ~255) + 32 * (o >> 6) + 16 * ((o >> 5) & 1), EH, (float)(1 << WSHIFT), scr, F.lane); } }
.LBB0_54:
	s_mul_hi_i32 s18, s91, 0xfb259c83
	s_lshr_b32 s26, s18, 31
	s_ashr_i32 s18, s18, 10
	s_add_i32 s18, s18, s26
	s_mul_hi_i32 s26, s91, 0x4da637d
	s_lshr_b32 s27, s26, 31
	s_ashr_i32 s26, s26, 10
	s_add_i32 s26, s26, s27
	s_add_i32 s18, s18, 1
	s_mul_i32 s26, s26, 0xd300
	s_sub_i32 s94, s91, s26
	s_mul_i32 s58, s18, 0x1a600000
	s_mul_hi_u32 s33, s18, 0x1a600000
	s_add_u32 s92, s3, s58
	s_addc_u32 s93, s36, s33
	s_cmp_lt_i32 s94, 0xc700
	s_mov_b64 s[26:27], -1
	s_cbranch_scc0 .LBB0_71
	s_cmp_lt_i32 s94, 0xc300
	s_cbranch_scc0 .LBB0_68
	s_sub_i32 s34, 0xc2ff, s94
	s_mul_hi_u32 s26, s34, 0xaaaaaaab
	s_lshr_b32 s26, s26, 9
	s_mul_i32 s27, s26, 0x300
	s_sub_i32 s59, s34, s27
	s_cmpk_gt_u32 s59, 0x1ff
	s_cbranch_scc1 .Lrm_down
	s_and_b32 s27, s59, 15
	s_lshl_b32 s27, s27, 4
	s_bfe_u32 s28, s59, 0x40004
	s_or_b32 s27, s27, s28
	s_and_b32 s59, s59, 0x300
	s_or_b32 s59, s59, s27
	s_branch .Lrm_done
.Lrm_down:
	s_and_b32 s27, s59, 3
	s_lshl_b32 s27, s27, 6
	s_bfe_u32 s28, s59, 0x60002
	s_or_b32 s27, s27, s28
	s_or_b32 s59, s27, 0x200
.Lrm_done:
	s_cmpk_gt_u32 s59, 0x1ff
	s_mov_b64 s[28:29], -1
	s_cbranch_scc0 .LBB0_62
	s_cmpk_gt_u32 s34, 0xbfff
	s_mov_b64 s[30:31], -1
	s_cbranch_scc0 .LBB0_59
	v_mov_b32_e32 v31, s37
	ds_read_b64 v[56:57], v31
	s_lshl_b64 s[28:29], s[18:19], 22
	s_waitcnt lgkmcnt(0)
	v_readfirstlane_b32 s30, v56
	v_readfirstlane_b32 s27, v57
	s_add_u32 s28, s30, s28
	s_addc_u32 s29, s27, s29
	s_mov_b64 s[30:31], 0
